# M2 epilogue: one vmcnt(0) before the first store retires the staged tiles, so the next unit's relaxed first waits no longer depend on the number of stores a wave issued (masked-off stores included)
# speedup vs baseline: 1.0033x; 1.0033x over previous
.LBB0_2961:
	v_lshl_or_b32 v2, v23, 8, v164
	s_lshl_b32 s22, s31, 10
	v_add_u32_e32 v22, s22, v163
	v_ashrrev_i32_e32 v3, 31, v2
	ds_read_b32 v176, v22
	ds_read_b32 v178, v22 offset:64
	ds_read_b32 v180, v22 offset:128
	ds_read_b32 v182, v22 offset:192
	ds_read_b32 v184, v22 offset:512
	ds_read_b32 v186, v22 offset:576
	ds_read_b32 v188, v22 offset:640
	ds_read_b32 v190, v22 offset:704
	ds_read_b32 v192, v22 offset:13568
	ds_read_b32 v194, v22 offset:13632
	ds_read_b32 v196, v22 offset:13696
	ds_read_b32 v198, v22 offset:13760
	ds_read_b32 v200, v22 offset:14080
	ds_read_b32 v202, v22 offset:14144
	ds_read_b32 v204, v22 offset:14208
	ds_read_b32 v206, v22 offset:14272
	v_mov_b32_e32 v177, v99
	v_mov_b32_e32 v179, v99
	v_mov_b32_e32 v181, v99
	v_mov_b32_e32 v183, v99
	v_mov_b32_e32 v185, v99
	v_mov_b32_e32 v187, v99
	v_mov_b32_e32 v189, v99
	v_mov_b32_e32 v191, v99
	s_waitcnt lgkmcnt(0)
	v_lshlrev_b64 v[140:141], 11, v[176:177]
	v_lshl_add_u64 v[140:141], s[12:13], 0, v[140:141]
	v_lshl_add_u64 v[140:141], v[2:3], 1, v[140:141]
	v_lshlrev_b64 v[142:143], 11, v[178:179]
	v_lshl_add_u64 v[142:143], s[12:13], 0, v[142:143]
	v_lshl_add_u64 v[142:143], v[2:3], 1, v[142:143]
	v_lshlrev_b64 v[144:145], 11, v[180:181]
	v_lshl_add_u64 v[144:145], s[12:13], 0, v[144:145]
	v_lshl_add_u64 v[144:145], v[2:3], 1, v[144:145]
	v_lshlrev_b64 v[146:147], 11, v[182:183]
	v_lshl_add_u64 v[146:147], s[12:13], 0, v[146:147]
	v_lshl_add_u64 v[146:147], v[2:3], 1, v[146:147]
	v_lshlrev_b64 v[148:149], 11, v[184:185]
	v_lshl_add_u64 v[148:149], s[12:13], 0, v[148:149]
	v_lshl_add_u64 v[148:149], v[2:3], 1, v[148:149]
	v_lshlrev_b64 v[150:151], 11, v[186:187]
	v_lshl_add_u64 v[150:151], s[12:13], 0, v[150:151]
	v_lshl_add_u64 v[150:151], v[2:3], 1, v[150:151]
	v_lshlrev_b64 v[152:153], 11, v[188:189]
	v_lshl_add_u64 v[152:153], s[12:13], 0, v[152:153]
	v_lshl_add_u64 v[152:153], v[2:3], 1, v[152:153]
	v_lshlrev_b64 v[154:155], 11, v[190:191]
	v_lshl_add_u64 v[154:155], s[12:13], 0, v[154:155]
	v_lshl_add_u64 v[154:155], v[2:3], 1, v[154:155]
	v_pk_add_f32 v[138:139], v[138:139], v[248:249]
	v_pk_add_f32 v[136:137], v[136:137], v[246:247]
	v_pk_add_f32 v[134:135], v[134:135], v[244:245]
	v_pk_add_f32 v[132:133], v[132:133], v[242:243]
	v_pk_add_f32 v[130:131], v[130:131], v[240:241]
	v_pk_add_f32 v[128:129], v[128:129], v[238:239]
	v_pk_add_f32 v[126:127], v[126:127], v[236:237]
	v_pk_add_f32 v[124:125], v[124:125], v[234:235]
	v_pk_mul_f32 v[138:139], v[138:139], v[192:193] op_sel_hi:[1,0]
	v_pk_mul_f32 v[136:137], v[136:137], v[192:193] op_sel_hi:[1,0]
	v_pk_mul_f32 v[134:135], v[134:135], v[192:193] op_sel_hi:[1,0]
	v_pk_mul_f32 v[132:133], v[132:133], v[192:193] op_sel_hi:[1,0]
	v_pk_mul_f32 v[130:131], v[130:131], v[192:193] op_sel_hi:[1,0]
	v_pk_mul_f32 v[128:129], v[128:129], v[192:193] op_sel_hi:[1,0]
	v_pk_mul_f32 v[210:211], v[126:127], v[192:193] op_sel_hi:[1,0]
	v_pk_mul_f32 v[208:209], v[124:125], v[192:193] op_sel_hi:[1,0]
	v_cvt_pk_bf16_f32 v124, v136, v137
	v_cvt_pk_bf16_f32 v125, v138, v139
	v_cvt_pk_bf16_f32 v126, v132, v133
	v_cvt_pk_bf16_f32 v127, v134, v135
	v_cvt_pk_bf16_f32 v128, v128, v129
	v_cvt_pk_bf16_f32 v129, v130, v131
	v_cvt_pk_bf16_f32 v130, v208, v209
	v_cvt_pk_bf16_f32 v131, v210, v211
	s_waitcnt vmcnt(0)
	v_cmp_lt_i32_e32 vcc, -1, v176
	s_and_saveexec_b64 s[38:39], vcc
	global_store_dwordx4 v[140:141], v[124:127], off
	global_store_dwordx4 v[140:141], v[128:131], off offset:256
	s_or_b64 exec, exec, s[38:39]
	v_pk_add_f32 v[122:123], v[122:123], v[248:249]
	v_pk_add_f32 v[120:121], v[120:121], v[246:247]
	v_pk_add_f32 v[118:119], v[118:119], v[244:245]
	v_pk_add_f32 v[116:117], v[116:117], v[242:243]
	v_pk_add_f32 v[114:115], v[114:115], v[240:241]
	v_pk_add_f32 v[112:113], v[112:113], v[238:239]
	v_pk_add_f32 v[110:111], v[110:111], v[236:237]
	v_pk_add_f32 v[108:109], v[108:109], v[234:235]
	v_pk_mul_f32 v[122:123], v[122:123], v[194:195] op_sel_hi:[1,0]
	v_pk_mul_f32 v[120:121], v[120:121], v[194:195] op_sel_hi:[1,0]
	v_pk_mul_f32 v[118:119], v[118:119], v[194:195] op_sel_hi:[1,0]
	v_pk_mul_f32 v[116:117], v[116:117], v[194:195] op_sel_hi:[1,0]
	v_pk_mul_f32 v[114:115], v[114:115], v[194:195] op_sel_hi:[1,0]
	v_pk_mul_f32 v[112:113], v[112:113], v[194:195] op_sel_hi:[1,0]
	v_pk_mul_f32 v[210:211], v[110:111], v[194:195] op_sel_hi:[1,0]
	v_pk_mul_f32 v[208:209], v[108:109], v[194:195] op_sel_hi:[1,0]
	v_cvt_pk_bf16_f32 v108, v120, v121
	v_cvt_pk_bf16_f32 v109, v122, v123
	v_cvt_pk_bf16_f32 v110, v116, v117
	v_cvt_pk_bf16_f32 v111, v118, v119
	v_cvt_pk_bf16_f32 v112, v112, v113
	v_cvt_pk_bf16_f32 v113, v114, v115
	v_cvt_pk_bf16_f32 v114, v208, v209
	v_cvt_pk_bf16_f32 v115, v210, v211
	v_cmp_lt_i32_e32 vcc, -1, v178
	s_and_saveexec_b64 s[38:39], vcc
	global_store_dwordx4 v[142:143], v[108:111], off
	global_store_dwordx4 v[142:143], v[112:115], off offset:256
	s_or_b64 exec, exec, s[38:39]
	v_pk_add_f32 v[106:107], v[106:107], v[248:249]
	v_pk_add_f32 v[104:105], v[104:105], v[246:247]
	v_pk_add_f32 v[102:103], v[102:103], v[244:245]
	v_pk_add_f32 v[100:101], v[100:101], v[242:243]
	v_pk_add_f32 v[94:95], v[94:95], v[240:241]
	v_pk_add_f32 v[92:93], v[92:93], v[238:239]
	v_pk_add_f32 v[90:91], v[90:91], v[236:237]
	v_pk_add_f32 v[88:89], v[88:89], v[234:235]
	v_pk_mul_f32 v[106:107], v[106:107], v[196:197] op_sel_hi:[1,0]
	v_pk_mul_f32 v[104:105], v[104:105], v[196:197] op_sel_hi:[1,0]
	v_pk_mul_f32 v[102:103], v[102:103], v[196:197] op_sel_hi:[1,0]
	v_pk_mul_f32 v[100:101], v[100:101], v[196:197] op_sel_hi:[1,0]
	v_pk_mul_f32 v[94:95], v[94:95], v[196:197] op_sel_hi:[1,0]
	v_pk_mul_f32 v[92:93], v[92:93], v[196:197] op_sel_hi:[1,0]
	v_pk_mul_f32 v[210:211], v[90:91], v[196:197] op_sel_hi:[1,0]
	v_pk_mul_f32 v[208:209], v[88:89], v[196:197] op_sel_hi:[1,0]
	v_cvt_pk_bf16_f32 v88, v104, v105
	v_cvt_pk_bf16_f32 v89, v106, v107
	v_cvt_pk_bf16_f32 v90, v100, v101
	v_cvt_pk_bf16_f32 v91, v102, v103
	v_cvt_pk_bf16_f32 v92, v92, v93
	v_cvt_pk_bf16_f32 v93, v94, v95
	v_cvt_pk_bf16_f32 v94, v208, v209
	v_cvt_pk_bf16_f32 v95, v210, v211
	v_cmp_lt_i32_e32 vcc, -1, v180
	s_and_saveexec_b64 s[38:39], vcc
	global_store_dwordx4 v[144:145], v[88:91], off
	global_store_dwordx4 v[144:145], v[92:95], off offset:256
	s_or_b64 exec, exec, s[38:39]
	v_pk_add_f32 v[86:87], v[86:87], v[248:249]
	v_pk_add_f32 v[84:85], v[84:85], v[246:247]
	v_pk_add_f32 v[82:83], v[82:83], v[244:245]
	v_pk_add_f32 v[80:81], v[80:81], v[242:243]
	v_pk_add_f32 v[78:79], v[78:79], v[240:241]
	v_pk_add_f32 v[76:77], v[76:77], v[238:239]
	v_pk_add_f32 v[74:75], v[74:75], v[236:237]
	v_pk_add_f32 v[72:73], v[72:73], v[234:235]
	v_pk_mul_f32 v[86:87], v[86:87], v[198:199] op_sel_hi:[1,0]
	v_pk_mul_f32 v[84:85], v[84:85], v[198:199] op_sel_hi:[1,0]
	v_pk_mul_f32 v[82:83], v[82:83], v[198:199] op_sel_hi:[1,0]
	v_pk_mul_f32 v[80:81], v[80:81], v[198:199] op_sel_hi:[1,0]
	v_pk_mul_f32 v[78:79], v[78:79], v[198:199] op_sel_hi:[1,0]
	v_pk_mul_f32 v[76:77], v[76:77], v[198:199] op_sel_hi:[1,0]
	v_pk_mul_f32 v[210:211], v[74:75], v[198:199] op_sel_hi:[1,0]
	v_pk_mul_f32 v[208:209], v[72:73], v[198:199] op_sel_hi:[1,0]
	v_cvt_pk_bf16_f32 v72, v84, v85
	v_cvt_pk_bf16_f32 v73, v86, v87
	v_cvt_pk_bf16_f32 v74, v80, v81
	v_cvt_pk_bf16_f32 v75, v82, v83
	v_cvt_pk_bf16_f32 v76, v76, v77
	v_cvt_pk_bf16_f32 v77, v78, v79
	v_cvt_pk_bf16_f32 v78, v208, v209
	v_cvt_pk_bf16_f32 v79, v210, v211
	v_cmp_lt_i32_e32 vcc, -1, v182
	s_and_saveexec_b64 s[38:39], vcc
	global_store_dwordx4 v[146:147], v[72:75], off
	global_store_dwordx4 v[146:147], v[76:79], off offset:256
	s_or_b64 exec, exec, s[38:39]
	v_pk_add_f32 v[70:71], v[70:71], v[248:249]
	v_pk_add_f32 v[68:69], v[68:69], v[246:247]
	v_pk_add_f32 v[66:67], v[66:67], v[244:245]
	v_pk_add_f32 v[64:65], v[64:65], v[242:243]
	v_pk_add_f32 v[62:63], v[62:63], v[240:241]
	v_pk_add_f32 v[60:61], v[60:61], v[238:239]
	v_pk_add_f32 v[58:59], v[58:59], v[236:237]
	v_pk_add_f32 v[56:57], v[56:57], v[234:235]
	v_pk_mul_f32 v[70:71], v[70:71], v[200:201] op_sel_hi:[1,0]
	v_pk_mul_f32 v[68:69], v[68:69], v[200:201] op_sel_hi:[1,0]
	v_pk_mul_f32 v[66:67], v[66:67], v[200:201] op_sel_hi:[1,0]
	v_pk_mul_f32 v[64:65], v[64:65], v[200:201] op_sel_hi:[1,0]
	v_pk_mul_f32 v[62:63], v[62:63], v[200:201] op_sel_hi:[1,0]
	v_pk_mul_f32 v[60:61], v[60:61], v[200:201] op_sel_hi:[1,0]
	v_pk_mul_f32 v[210:211], v[58:59], v[200:201] op_sel_hi:[1,0]
	v_pk_mul_f32 v[208:209], v[56:57], v[200:201] op_sel_hi:[1,0]
	v_cvt_pk_bf16_f32 v56, v68, v69
	v_cvt_pk_bf16_f32 v57, v70, v71
	v_cvt_pk_bf16_f32 v58, v64, v65
	v_cvt_pk_bf16_f32 v59, v66, v67
	v_cvt_pk_bf16_f32 v60, v60, v61
	v_cvt_pk_bf16_f32 v61, v62, v63
	v_cvt_pk_bf16_f32 v62, v208, v209
	v_cvt_pk_bf16_f32 v63, v210, v211
	v_cmp_lt_i32_e32 vcc, -1, v184
	s_and_saveexec_b64 s[38:39], vcc
	global_store_dwordx4 v[148:149], v[56:59], off
	global_store_dwordx4 v[148:149], v[60:63], off offset:256
	s_or_b64 exec, exec, s[38:39]
	v_pk_add_f32 v[54:55], v[54:55], v[248:249]
	v_pk_add_f32 v[52:53], v[52:53], v[246:247]
	v_pk_add_f32 v[50:51], v[50:51], v[244:245]
	v_pk_add_f32 v[48:49], v[48:49], v[242:243]
	v_pk_add_f32 v[46:47], v[46:47], v[240:241]
	v_pk_add_f32 v[44:45], v[44:45], v[238:239]
	v_pk_add_f32 v[42:43], v[42:43], v[236:237]
	v_pk_add_f32 v[40:41], v[40:41], v[234:235]
	v_pk_mul_f32 v[54:55], v[54:55], v[202:203] op_sel_hi:[1,0]
	v_pk_mul_f32 v[52:53], v[52:53], v[202:203] op_sel_hi:[1,0]
	v_pk_mul_f32 v[50:51], v[50:51], v[202:203] op_sel_hi:[1,0]
	v_pk_mul_f32 v[48:49], v[48:49], v[202:203] op_sel_hi:[1,0]
	v_pk_mul_f32 v[46:47], v[46:47], v[202:203] op_sel_hi:[1,0]
	v_pk_mul_f32 v[44:45], v[44:45], v[202:203] op_sel_hi:[1,0]
	v_pk_mul_f32 v[210:211], v[42:43], v[202:203] op_sel_hi:[1,0]
	v_pk_mul_f32 v[208:209], v[40:41], v[202:203] op_sel_hi:[1,0]
	v_cvt_pk_bf16_f32 v40, v52, v53
	v_cvt_pk_bf16_f32 v41, v54, v55
	v_cvt_pk_bf16_f32 v42, v48, v49
	v_cvt_pk_bf16_f32 v43, v50, v51
	v_cvt_pk_bf16_f32 v44, v44, v45
	v_cvt_pk_bf16_f32 v45, v46, v47
	v_cvt_pk_bf16_f32 v46, v208, v209
	v_cvt_pk_bf16_f32 v47, v210, v211
	v_cmp_lt_i32_e32 vcc, -1, v186
	s_and_saveexec_b64 s[38:39], vcc
	global_store_dwordx4 v[150:151], v[40:43], off
	global_store_dwordx4 v[150:151], v[44:47], off offset:256
	s_or_b64 exec, exec, s[38:39]
	v_pk_add_f32 v[38:39], v[38:39], v[248:249]
	v_pk_add_f32 v[36:37], v[36:37], v[246:247]
	v_pk_add_f32 v[34:35], v[34:35], v[244:245]
	v_pk_add_f32 v[32:33], v[32:33], v[242:243]
	v_pk_add_f32 v[30:31], v[30:31], v[240:241]
	v_pk_add_f32 v[28:29], v[28:29], v[238:239]
	v_pk_add_f32 v[26:27], v[26:27], v[236:237]
	v_pk_add_f32 v[24:25], v[24:25], v[234:235]
	v_pk_mul_f32 v[38:39], v[38:39], v[204:205] op_sel_hi:[1,0]
	v_pk_mul_f32 v[36:37], v[36:37], v[204:205] op_sel_hi:[1,0]
	v_pk_mul_f32 v[34:35], v[34:35], v[204:205] op_sel_hi:[1,0]
	v_pk_mul_f32 v[32:33], v[32:33], v[204:205] op_sel_hi:[1,0]
	v_pk_mul_f32 v[30:31], v[30:31], v[204:205] op_sel_hi:[1,0]
	v_pk_mul_f32 v[28:29], v[28:29], v[204:205] op_sel_hi:[1,0]
	v_pk_mul_f32 v[210:211], v[26:27], v[204:205] op_sel_hi:[1,0]
	v_pk_mul_f32 v[208:209], v[24:25], v[204:205] op_sel_hi:[1,0]
	v_cvt_pk_bf16_f32 v24, v36, v37
	v_cvt_pk_bf16_f32 v25, v38, v39
	v_cvt_pk_bf16_f32 v26, v32, v33
	v_cvt_pk_bf16_f32 v27, v34, v35
	v_cvt_pk_bf16_f32 v28, v28, v29
	v_cvt_pk_bf16_f32 v29, v30, v31
	v_cvt_pk_bf16_f32 v30, v208, v209
	v_cvt_pk_bf16_f32 v31, v210, v211
	v_cmp_lt_i32_e32 vcc, -1, v188
	s_and_saveexec_b64 s[38:39], vcc
	global_store_dwordx4 v[152:153], v[24:27], off
	global_store_dwordx4 v[152:153], v[28:31], off offset:256
	s_or_b64 exec, exec, s[38:39]
	v_pk_add_f32 v[20:21], v[20:21], v[248:249]
	v_pk_add_f32 v[18:19], v[18:19], v[246:247]
	v_pk_add_f32 v[16:17], v[16:17], v[244:245]
	v_pk_add_f32 v[14:15], v[14:15], v[242:243]
	v_pk_add_f32 v[12:13], v[12:13], v[240:241]
	v_pk_add_f32 v[10:11], v[10:11], v[238:239]
	v_pk_add_f32 v[8:9], v[8:9], v[236:237]
	v_pk_add_f32 v[6:7], v[6:7], v[234:235]
	v_pk_mul_f32 v[20:21], v[20:21], v[206:207] op_sel_hi:[1,0]
	v_pk_mul_f32 v[18:19], v[18:19], v[206:207] op_sel_hi:[1,0]
	v_pk_mul_f32 v[16:17], v[16:17], v[206:207] op_sel_hi:[1,0]
	v_pk_mul_f32 v[14:15], v[14:15], v[206:207] op_sel_hi:[1,0]
	v_pk_mul_f32 v[12:13], v[12:13], v[206:207] op_sel_hi:[1,0]
	v_pk_mul_f32 v[10:11], v[10:11], v[206:207] op_sel_hi:[1,0]
	v_pk_mul_f32 v[210:211], v[8:9], v[206:207] op_sel_hi:[1,0]
	v_pk_mul_f32 v[208:209], v[6:7], v[206:207] op_sel_hi:[1,0]
	v_cvt_pk_bf16_f32 v6, v18, v19
	v_cvt_pk_bf16_f32 v7, v20, v21
	v_cvt_pk_bf16_f32 v8, v14, v15
	v_cvt_pk_bf16_f32 v9, v16, v17
	v_cvt_pk_bf16_f32 v10, v10, v11
	v_cvt_pk_bf16_f32 v11, v12, v13
	v_cvt_pk_bf16_f32 v12, v208, v209
	v_cvt_pk_bf16_f32 v13, v210, v211
	v_cmp_lt_i32_e32 vcc, -1, v190
	s_and_saveexec_b64 s[38:39], vcc
	global_store_dwordx4 v[154:155], v[6:9], off
	global_store_dwordx4 v[154:155], v[10:13], off offset:256
